# combo5: light-tile loops also skip A DMA piece 0 for wave pairs whose 16 rows lie beyond the tile row count
# speedup vs baseline: 1.0166x; 1.0052x over previous
; __device__ __forceinline__ int tid_opaque() { int t = threadIdx.x; asm volatile("" : "+v"(t)); return t; }
;     __device__ __forceinline__ void init() {
;         const int tid = tid_opaque(), wid = tid >> 6, lane = tid & 63;
;         wr = wid >> 2; wc = wid & 3; fr = lane & 15; fq = lane >> 4;
;         aR = (wid >> 1) * 16 + (lane >> 2); aC = (wid & 1) * 32 + (((lane & 3) ^ ((lane >> 5) << 1)) * 8);
;         a_w = (unsigned)(wid * 1024 + lane * 16);
;         { const int l32 = lane & 31, kc8 = 2 * (wid >> 1) + (lane >> 5), wc_ = l32 >> 3, bfq = (l32 >> 1) & 3, nlo = l32 & 1; b_p = wid & 1;
;           b_k = kc8 * 8; b_col = wc_ * 64 + b_p * 32 + bfq * 8 + nlo * 4; b_gucol = wc_ * 32 + bfq * 8 + nlo * 4;
;           const int sub = wc_ * 4 + 2 * b_p + nlo;
;           b_w = (unsigned)((sub * 2 + (kc8 >> 2)) * 1024 + (((4 * bfq) * 64 + (kc8 & 3) * 16) ^ ((bfq >> 1) << 5))); b_rot = (unsigned)(nlo * 64); }
;         const unsigned lo = (unsigned)((fr * 64 + fq * 16) ^ ((fr >> 3) << 5));
;         a_r = (unsigned)(wr * 16384) + lo; b_r = 32768u + (unsigned)(wc * 8192) + lo;
; __device__ __forceinline__ void phase_moe_gu(const Ptrs& p, LAS unsigned char* lds) {
;     ...
;         GemmT T; T.init();
;         const int* list = (const int*)(p.ws + OFF_LIST) + (size_t)mu.e * NTOK; const int i0 = mu.mt * 256, n0 = mu.nt * 128;
;         unsigned ao[4];
; #pragma unroll
;         for (int i = 0; i < 4; ++i) { const int r = i0 + T.aR + 64 * i; const int tok = (r < mu.cnt) ? (list[r] >> 2) : 0; ao[i] = (unsigned)((tok * D + T.aC) * 2); }
;         const float* wsel = ((__builtin_amdgcn_readfirstlane(T.b_p) & 1) ? p.w_up : p.w_gate) + (size_t)mu.e * D * D + n0;
;         const unsigned bo = (unsigned)((T.b_k * D + T.b_gucol) * 4);
;         f32x4 acc[8][4]; acc_zero(acc);
;         const int mlim = __builtin_amdgcn_readfirstlane(T.wr) ? 0 : ((mu.cnt - i0 + 15) >> 4);
.LBB0_1163:
	s_andn2_b64 vcc, exec, s[0:1]
	s_mov_b64 s[0:1], -1
	s_cbranch_vccnz .LBB0_1005
	s_ashr_i32 s43, s42, 31
	s_lshl_b64 s[0:1], s[42:43], 15
	v_mov_b32_e32 v3, v0
	s_add_u32 s0, s52, s0
	s_addc_u32 s1, s53, s1
	v_bfe_u32 v4, v3, 2, 4
	s_lshl_b32 s2, s86, 8
	v_ashrrev_i32_e32 v10, 7, v3
	v_or_b32_e32 v4, s2, v4
	v_lshl_add_u32 v4, v10, 4, v4
	v_cmp_gt_i32_e32 vcc, s87, v4
	v_mov_b32_e32 v6, 0
	v_ashrrev_i32_e32 v5, 31, v4
	v_mov_b32_e32 v7, 0
	v_mov_b32_e32 v8, 0
	v_mov_b32_e32 v9, 0
	v_lshl_add_u64 v[12:13], v[4:5], 2, s[0:1]
	s_and_saveexec_b64 s[4:5], vcc
	global_load_dword v7, v[12:13], off
	s_or_b64 exec, exec, s[4:5]
	v_add_u32_e32 v11, 64, v4
	v_cmp_gt_i32_e32 vcc, s87, v11
	s_and_saveexec_b64 s[4:5], vcc
	global_load_dword v6, v[12:13], off offset:256
	s_or_b64 exec, exec, s[4:5]
	v_add_u32_e32 v11, 0x80, v4
	v_cmp_gt_i32_e32 vcc, s87, v11
	s_and_saveexec_b64 s[4:5], vcc
	global_load_dword v9, v[12:13], off offset:512
	s_or_b64 exec, exec, s[4:5]
	v_add_u32_e32 v11, 0xc0, v4
	v_cmp_gt_i32_e32 vcc, s87, v11
	s_and_saveexec_b64 s[4:5], vcc
	global_load_dword v8, v[12:13], off offset:768
	s_or_b64 exec, exec, s[4:5]
	v_ashrrev_i32_e32 v5, 6, v3
	v_and_b32_e32 v11, 1, v5
	s_lshl_b32 s0, s85, 7
	v_readfirstlane_b32 s1, v11
	v_readlane_b32 s4, v246, 0
	s_bitcmp0_b32 s1, 0
	v_readlane_b32 s5, v246, 1
	s_cselect_b32 s1, s49, s5
	s_cselect_b32 s3, s48, s4
	s_lshl_b64 s[4:5], s[42:43], 24
	v_readlane_b32 s6, v246, 2
	s_add_u32 s3, s3, s4
	v_and_b32_e32 v4, 63, v3
	s_addc_u32 s6, s1, s5
	s_ashr_i32 s1, s0, 31
	v_lshrrev_b32_e32 v12, 5, v4
	v_bfe_u32 v13, v3, 1, 2
	s_lshl_b64 s[4:5], s[0:1], 2
	v_lshl_or_b32 v10, v10, 1, v12
	v_bfe_u32 v12, v3, 3, 2
	v_and_b32_e32 v14, 1, v3
	v_lshlrev_b32_e32 v15, 5, v13
	s_add_u32 s24, s3, s4
	v_lshl_or_b32 v15, v12, 7, v15
	v_lshlrev_b32_e32 v16, 16, v10
	v_lshlrev_b32_e32 v17, 4, v14
	s_addc_u32 s1, s6, s5
	v_or3_b32 v225, v15, v17, v16
	s_and_b32 s25, s1, 0xffff
	s_movk_i32 s1, 0x2000
	buffer_load_dwordx4 v[114:117], v225, s[24:27], 0 offen
	buffer_load_dwordx4 v[118:121], v225, s[24:27], s66 offen
	s_mov_b32 s3, 0x8000
	buffer_load_dwordx4 v[126:129], v225, s[24:27], s1 offen
	buffer_load_dwordx4 v[122:125], v225, s[24:27], s3 offen
	s_movk_i32 s1, 0x4000
	s_mov_b32 s3, 0xa000
	buffer_load_dwordx4 v[130:133], v225, s[24:27], s1 offen
	buffer_load_dwordx4 v[134:137], v225, s[24:27], s3 offen
	s_mov_b32 s1, 0xc000
	s_mov_b32 s3, 0xe000
	buffer_load_dwordx4 v[142:145], v225, s[24:27], s1 offen
	buffer_load_dwordx4 v[146:149], v225, s[24:27], s3 offen
	s_waitcnt vmcnt(8)
	v_lshlrev_b32_e32 v7, 10, v7
	v_and_b32_e32 v7, 0xfffff000, v7
	v_lshlrev_b32_e32 v6, 10, v6
	v_and_b32_e32 v6, 0xfffff000, v6
	v_lshlrev_b32_e32 v9, 10, v9
	v_and_b32_e32 v9, 0xfffff000, v9
	v_lshlrev_b32_e32 v8, 10, v8
	v_and_b32_e32 v8, 0xfffff000, v8
	v_lshlrev_b32_e32 v17, 4, v3
	v_lshlrev_b32_e32 v15, 6, v11
	v_and_b32_e32 v16, 32, v3
	v_and_b32_e32 v17, 48, v17
	v_bitop3_b32 v15, v17, v15, v16 bitop3:0xde
	v_or_b32_e32 v221, v9, v15
	v_lshlrev_b32_e32 v9, 2, v12
	v_lshlrev_b32_e32 v11, 1, v11
	v_or3_b32 v9, v9, v11, v14
	v_lshlrev_b32_e32 v11, 2, v3
	v_and_b32_e32 v12, 0xfffffc00, v11
	v_lshl_add_u32 v9, v9, 11, v12
	v_lshlrev_b32_e32 v12, 8, v13
	v_lshlrev_b32_e32 v10, 4, v10
	v_and_or_b32 v10, v10, 48, v12
	v_lshlrev_b32_e32 v12, 3, v3
	v_or_b32_e32 v223, v7, v15
	v_and_b32_e32 v7, 15, v3
	v_and_b32_e32 v12, 32, v12
	v_or_b32_e32 v222, v6, v15
	v_ashrrev_i32_e32 v6, 8, v3
	v_bitop3_b32 v219, v9, v10, v12 bitop3:0xf6
	v_lshlrev_b32_e32 v7, 6, v7
	v_and_b32_e32 v3, 48, v3
	v_and_b32_e32 v10, 32, v11
	v_or_b32_e32 v9, v7, v3
	v_bitop3_b32 v3, v7, v10, v3 bitop3:0x36
	v_lshlrev_b32_e32 v11, 13, v5
	v_lshlrev_b32_e32 v220, 6, v14
	v_lshlrev_b32_e32 v4, 4, v4
	v_lshlrev_b32_e32 v7, 14, v6
	v_and_or_b32 v226, v11, s66, v3
	v_cmp_eq_u32_e32 vcc, 0, v215
	v_add_u32_e32 v227, 0, v219
	v_add_u32_e32 v3, 0xc0, v220
	v_or_b32_e32 v224, v8, v15
	v_lshl_or_b32 v229, v5, 10, v4
	v_bitop3_b32 v216, v9, v7, v10 bitop3:0xde
	v_or_b32_e32 v217, 0x8000, v226
	v_readfirstlane_b32 s1, v6
	s_and_b64 vcc, exec, vcc
	v_add_u32_e32 v228, v227, v220
	v_and_b32_e32 v218, 0xc0, v3
	v_readlane_b32 s7, v246, 3
	v_readlane_b32 s8, v246, 4
	v_readlane_b32 s9, v246, 5
	v_readlane_b32 s10, v246, 6
	v_readlane_b32 s11, v246, 7
	s_cbranch_vccnz .LBB0_1263
; #define G_DMA_A(buf, t, i_) __builtin_amdgcn_raw_ptr_buffer_load_lds(ra, (LAS void*)(lds + (buf) * 65536 + a_wu + (i_) * 8192), 16, ao##i_, (unsigned)(t) * 128u, 0, 0)
; #define G_ISSUE_B(t) do { const unsigned so_ = (unsigned)(t) * 64u * ldbB; _Pragma("unroll") for (int i_ = 0; i_ < 8; ++i_) sb[i_] = __builtin_bit_cast(f32x4, __builtin_amdgcn_raw_buffer_load_b128(rb, bo, so_ + (unsigned)i_ * ldbB, 0)); } while (0)
; #define G_RETIRE() asm volatile("s_waitcnt vmcnt(0)" : "+v"(sb[0]), "+v"(sb[1]), "+v"(sb[2]), "+v"(sb[3]), "+v"(sb[4]), "+v"(sb[5]), "+v"(sb[6]), "+v"(sb[7]) :: "memory")
; #define G_WRITE_B(buf) do { LAS unsigned char* d_ = lds + (buf) * 65536; \
;         _Pragma("unroll") for (int j_ = 0; j_ < 4; ++j_) { u32x4 w_; w_.x = cvtpk(sb[0][j_], sb[1][j_]); w_.y = cvtpk(sb[2][j_], sb[3][j_]); w_.z = cvtpk(sb[4][j_], sb[5][j_]); w_.w = cvtpk(sb[6][j_], sb[7][j_]); \
;             *(LAS u32x4*)(d_ + 32768 + T.b_w + ((T.b_rot + 64u * j_) & 255u)) = w_; } } while (0)
; #define G_BAR() do { asm volatile("s_waitcnt lgkmcnt(0)" ::: "memory"); __builtin_amdgcn_s_barrier(); asm volatile("" ::: "memory"); } while (0)
; #define G_DMA_A(buf, t, i_) __builtin_amdgcn_raw_ptr_buffer_load_lds(ra, (LAS void*)(lds + (buf) * 65536 + a_wu + (i_) * 8192), 16, ao##i_, (unsigned)(t) * 128u, 0, 0)
; #define G_ISSUE_B(t) do { const unsigned so_ = (unsigned)(t) * 64u * ldbB; _Pragma("unroll") for (int i_ = 0; i_ < 8; ++i_) sb[i_] = __builtin_bit_cast(f32x4, __builtin_amdgcn_raw_buffer_load_b128(rb, bo, so_ + (unsigned)i_ * ldbB, 0)); } while (0)
; #define G_RETIRE() asm volatile("s_waitcnt vmcnt(0)" : "+v"(sb[0]), "+v"(sb[1]), "+v"(sb[2]), "+v"(sb[3]), "+v"(sb[4]), "+v"(sb[5]), "+v"(sb[6]), "+v"(sb[7]) :: "memory")
; __device__ __forceinline__ void gemm_kloop_light(f32x4 (&acc)[8][4], LAS unsigned char* lds, const GemmT& T, ...
;     ...
;     G_ISSUE_B(0); G_DMA_A(0, 0, 0); G_DMA_A(0, 0, 1); G_DMA_A(0, 0, 2); G_DMA_A(0, 0, 3); G_RETIRE(); G_WRITE_B(0);
;     if (nt > 1) G_ISSUE_B(1);
;     G_BAR();
; __device__ __forceinline__ void phase_moe_gu(const Ptrs& p, LAS unsigned char* lds) {
;     ...
;         f32x4 acc[8][4]; acc_zero(acc);
;         const int mlim = __builtin_amdgcn_readfirstlane(T.wr) ? 0 : ((mu.cnt - i0 + 15) >> 4);
;         if (mu.light) gemm_kloop_light(acc, lds, T, mk_rsrc(h2), ao[0], ao[1], ao[2], ao[3], mk_rsrc(wsel), bo, D * 4u, D / 64, mlim);
	s_sub_i32 s3, s87, s2
	s_mov_b32 s99, s3
	v_readfirstlane_b32 s100, v0
	s_nop 3
	s_lshr_b32 s100, s100, 7
	s_lshl_b32 s100, s100, 4
	s_add_i32 s3, s3, 15
	s_ashr_i32 s3, s3, 4
	s_cmp_eq_u32 s1, 0
	s_cselect_b32 s1, s3, 0
	v_readfirstlane_b32 s3, v229
	s_and_b32 s3, s3, 0xfffffc00
	s_add_i32 s3, s3, 0
	s_mov_b32 s38, s26
	s_mov_b32 s39, s27
	s_mov_b32 m0, s3
	s_waitcnt vmcnt(6)
	v_mov_b64_e32 v[4:5], v[118:119]
	buffer_load_dwordx4 v223, s[36:39], 0 offen lds
	s_add_i32 m0, s3, 0x2000
	s_waitcnt vmcnt(3)
	v_mov_b64_e32 v[8:9], v[134:135]
	buffer_load_dwordx4 v222, s[36:39], 0 offen lds
	s_add_i32 m0, s3, 0x4000
	v_mov_b64_e32 v[12:13], v[114:115]
	buffer_load_dwordx4 v221, s[36:39], 0 offen lds
	s_add_i32 m0, s3, 0x6000
	s_waitcnt vmcnt(3)
	v_mov_b64_e32 v[16:17], v[146:147]
	v_mov_b64_e32 v[20:21], v[130:131]
	v_mov_b64_e32 v[24:25], v[122:123]
	v_mov_b64_e32 v[28:29], v[142:143]
	v_mov_b64_e32 v[32:33], v[126:127]
	buffer_load_dwordx4 v224, s[36:39], 0 offen lds
	v_mov_b64_e32 v[6:7], v[120:121]
	v_mov_b64_e32 v[10:11], v[136:137]
	v_mov_b64_e32 v[14:15], v[116:117]
	v_mov_b64_e32 v[18:19], v[148:149]
	v_mov_b64_e32 v[22:23], v[132:133]
	v_mov_b64_e32 v[26:27], v[124:125]
	v_mov_b64_e32 v[30:31], v[144:145]
	v_mov_b64_e32 v[34:35], v[128:129]
	s_waitcnt vmcnt(0)
	buffer_load_dwordx4 v[162:165], v225, s[24:27], s67 offen
	buffer_load_dwordx4 v[166:169], v225, s[24:27], s76 offen
	buffer_load_dwordx4 v[170:173], v225, s[24:27], s77 offen
	buffer_load_dwordx4 v[174:177], v225, s[24:27], s78 offen
	buffer_load_dwordx4 v[178:181], v225, s[24:27], s79 offen
	buffer_load_dwordx4 v[182:185], v225, s[24:27], s80 offen
	buffer_load_dwordx4 v[186:189], v225, s[24:27], s81 offen
	buffer_load_dwordx4 v[190:193], v225, s[24:27], s82 offen
	s_cmp_gt_i32 s1, 0
	s_cselect_b64 s[62:63], -1, 0
	s_cmp_lg_u32 s1, 1
	v_cvt_pk_bf16_f32 v36, v12, v32
	v_cvt_pk_bf16_f32 v37, v20, v4
	v_cvt_pk_bf16_f32 v38, v24, v8
	v_cvt_pk_bf16_f32 v39, v28, v16
	s_cselect_b64 s[60:61], -1, 0
	s_cmp_gt_i32 s1, 2
	ds_write_b128 v228, v[36:39] offset:32768
	v_cvt_pk_bf16_f32 v36, v13, v33
	v_cvt_pk_bf16_f32 v37, v21, v5
	v_cvt_pk_bf16_f32 v38, v25, v9
	v_cvt_pk_bf16_f32 v39, v29, v17
	s_cselect_b64 s[58:59], -1, 0
	s_cmp_gt_i32 s1, 3
	ds_write_b128 v228, v[36:39] offset:32832
	v_cvt_pk_bf16_f32 v36, v14, v34
	v_cvt_pk_bf16_f32 v37, v22, v6
	v_cvt_pk_bf16_f32 v38, v26, v10
	v_cvt_pk_bf16_f32 v39, v30, v18
	v_cvt_pk_bf16_f32 v4, v15, v35
	v_cvt_pk_bf16_f32 v5, v23, v7
	v_cvt_pk_bf16_f32 v6, v27, v11
	v_cvt_pk_bf16_f32 v7, v31, v19
	v_add_u32_e32 v3, v227, v218
	s_cselect_b64 s[54:55], -1, 0
	s_cmp_gt_i32 s1, 4
	ds_write_b128 v228, v[36:39] offset:32896
	ds_write_b128 v3, v[4:7] offset:32768
	s_cselect_b64 s[46:47], -1, 0
	s_cmp_gt_i32 s1, 5
	s_waitcnt lgkmcnt(0)
	s_barrier
	s_cselect_b64 s[44:45], -1, 0
	s_cmp_gt_i32 s1, 6
	v_mov_b32_e32 v4, v2
	v_mov_b32_e32 v5, v2
	s_cselect_b64 s[34:35], -1, 0
	s_cmp_gt_i32 s1, 7
	v_mov_b32_e32 v3, v2
	v_mov_b64_e32 v[16:17], v[4:5]
	v_mov_b64_e32 v[8:9], v[4:5]
	v_mov_b64_e32 v[20:21], v[4:5]
	v_mov_b64_e32 v[12:13], v[4:5]
	v_mov_b64_e32 v[32:33], v[4:5]
	v_mov_b64_e32 v[24:25], v[4:5]
	v_mov_b64_e32 v[36:37], v[4:5]
	v_mov_b64_e32 v[28:29], v[4:5]
	v_mov_b64_e32 v[48:49], v[4:5]
	v_mov_b64_e32 v[40:41], v[4:5]
	v_mov_b64_e32 v[52:53], v[4:5]
	v_mov_b64_e32 v[44:45], v[4:5]
	v_mov_b64_e32 v[64:65], v[4:5]
	v_mov_b64_e32 v[56:57], v[4:5]
	v_mov_b64_e32 v[68:69], v[4:5]
	v_mov_b64_e32 v[60:61], v[4:5]
	v_mov_b64_e32 v[80:81], v[4:5]
	v_mov_b64_e32 v[72:73], v[4:5]
	v_mov_b64_e32 v[84:85], v[4:5]
	v_mov_b64_e32 v[76:77], v[4:5]
	v_mov_b64_e32 v[96:97], v[4:5]
	v_mov_b64_e32 v[88:89], v[4:5]
	v_mov_b64_e32 v[100:101], v[4:5]
	v_mov_b64_e32 v[92:93], v[4:5]
	v_mov_b64_e32 v[112:113], v[4:5]
	v_mov_b64_e32 v[104:105], v[4:5]
	v_mov_b64_e32 v[140:141], v[4:5]
	v_mov_b64_e32 v[108:109], v[4:5]
	v_mov_b64_e32 v[160:161], v[4:5]
	v_mov_b64_e32 v[152:153], v[4:5]
	v_mov_b64_e32 v[196:197], v[4:5]
	v_mov_b64_e32 v[156:157], v[4:5]
	s_mov_b32 s68, 0
	s_cselect_b64 s[22:23], -1, 0
	s_mov_b32 s69, 0x10e000
	s_movk_i32 s70, 0x80
	v_mov_b64_e32 v[14:15], v[2:3]
	v_mov_b64_e32 v[6:7], v[2:3]
	v_mov_b64_e32 v[18:19], v[2:3]
	v_mov_b64_e32 v[10:11], v[2:3]
	v_mov_b64_e32 v[30:31], v[2:3]
	v_mov_b64_e32 v[22:23], v[2:3]
	v_mov_b64_e32 v[34:35], v[2:3]
	v_mov_b64_e32 v[26:27], v[2:3]
	v_mov_b64_e32 v[46:47], v[2:3]
	v_mov_b64_e32 v[38:39], v[2:3]
	v_mov_b64_e32 v[50:51], v[2:3]
	v_mov_b64_e32 v[42:43], v[2:3]
	v_mov_b64_e32 v[62:63], v[2:3]
	v_mov_b64_e32 v[54:55], v[2:3]
	v_mov_b64_e32 v[66:67], v[2:3]
	v_mov_b64_e32 v[58:59], v[2:3]
	v_mov_b64_e32 v[78:79], v[2:3]
	v_mov_b64_e32 v[70:71], v[2:3]
	v_mov_b64_e32 v[82:83], v[2:3]
	v_mov_b64_e32 v[74:75], v[2:3]
	v_mov_b64_e32 v[94:95], v[2:3]
	v_mov_b64_e32 v[86:87], v[2:3]
	v_mov_b64_e32 v[98:99], v[2:3]
	v_mov_b64_e32 v[90:91], v[2:3]
	v_mov_b64_e32 v[110:111], v[2:3]
	v_mov_b64_e32 v[102:103], v[2:3]
	v_mov_b64_e32 v[138:139], v[2:3]
	v_mov_b64_e32 v[106:107], v[2:3]
	v_mov_b64_e32 v[158:159], v[2:3]
	v_mov_b64_e32 v[150:151], v[2:3]
	v_mov_b64_e32 v[194:195], v[2:3]
	v_mov_b64_e32 v[154:155], v[2:3]
	s_branch .LBB0_1175

; #define G_DMA_A(buf, t, i_) __builtin_amdgcn_raw_ptr_buffer_load_lds(ra, (LAS void*)(lds + (buf) * 65536 + a_wu + (i_) * 8192), 16, ao##i_, (unsigned)(t) * 128u, 0, 0)
; #define G_DMA_A(buf, t, i_) __builtin_amdgcn_raw_ptr_buffer_load_lds(ra, (LAS void*)(lds + (buf) * 65536 + a_wu + (i_) * 8192), 16, ao##i_, (unsigned)(t) * 128u, 0, 0)
; __device__ __forceinline__ void gemm_kloop_light(f32x4 (&acc)[8][4], LAS unsigned char* lds, const GemmT& T, ...
;     ...
;     for (int t = 0; t < nt; ++t) { const int cur = t & 1; const bool w1 = t + 1 < nt, i2 = t + 2 < nt;
;         if (w1) { G_DMA_A(cur ^ 1, t + 1, 0); G_DMA_A(cur ^ 1, t + 1, 1); G_DMA_A(cur ^ 1, t + 1, 2); G_DMA_A(cur ^ 1, t + 1, 3); }
;         if (mlim > 0) {
.LBB0_1175:
	s_and_b32 s6, s68, 0x10000
	s_xor_b32 s71, s6, 0x10000
	s_add_i32 s4, s3, s71
	s_mov_b32 m0, s4
	s_add_i32 s5, s4, 0x6000
	s_add_i32 s7, s4, 0x4000
	s_addk_i32 s4, 0x2000
	s_cmp_le_i32 s99, s100
	s_cbranch_scc1 .Lmy_lsz0
	buffer_load_dwordx4 v223, s[36:39], s70 offen lds
.Lmy_lsz0:
	s_mov_b32 m0, s4
	v_cndmask_b32_e64 v3, 0, 1, s[62:63]
	s_cmp_lt_i32 s99, 65
	s_cbranch_scc1 .Lmy_lsk0
	buffer_load_dwordx4 v222, s[36:39], s70 offen lds

; #define G_DMA_A(buf, t, i_) __builtin_amdgcn_raw_ptr_buffer_load_lds(ra, (LAS void*)(lds + (buf) * 65536 + a_wu + (i_) * 8192), 16, ao##i_, (unsigned)(t) * 128u, 0, 0)
; #define G_DMA_A(buf, t, i_) __builtin_amdgcn_raw_ptr_buffer_load_lds(ra, (LAS void*)(lds + (buf) * 65536 + a_wu + (i_) * 8192), 16, ao##i_, (unsigned)(t) * 128u, 0, 0)
; __device__ __forceinline__ void gemm_kloop_light(f32x4 (&acc)[8][4], LAS unsigned char* lds, const GemmT& T, ...
;     ...
;     for (int t = 0; t < nt; ++t) { const int cur = t & 1; const bool w1 = t + 1 < nt, i2 = t + 2 < nt;
;         if (w1) { G_DMA_A(cur ^ 1, t + 1, 0); G_DMA_A(cur ^ 1, t + 1, 1); G_DMA_A(cur ^ 1, t + 1, 2); G_DMA_A(cur ^ 1, t + 1, 3); }
;         if (mlim > 0) {
.LBB0_1204:
	s_add_i32 m0, s3, 0x10000
	s_add_i32 s6, s3, 0x16000
	s_add_i32 s7, s3, 0x14000
	s_add_i32 s3, s3, 0x12000
	s_mov_b32 s38, s26
	s_mov_b32 s39, s27
	s_cmp_le_i32 s99, s100
	s_cbranch_scc1 .Lmy_lsz1
	buffer_load_dwordx4 v223, s[36:39], s83 offen lds
.Lmy_lsz1:
	s_mov_b32 m0, s3
	v_cndmask_b32_e64 v3, 0, 1, s[60:61]
	s_cmp_lt_i32 s99, 65
	s_cbranch_scc1 .Lmy_lsk1
	buffer_load_dwordx4 v222, s[36:39], s83 offen lds

; __device__ __forceinline__ int tid_opaque() { int t = threadIdx.x; asm volatile("" : "+v"(t)); return t; }
; __device__ __forceinline__ __amdgpu_buffer_rsrc_t mk_rsrc(const void* p) { return __builtin_amdgcn_make_buffer_rsrc((void*)p, 0, 0x7ffffff0, 0x00020000); }
; __device__ __forceinline__ void phase_moe_down(const Ptrs& p, LAS unsigned char* lds) {
;     ...
;         GemmT T; T.init();
;         const int* list = (const int*)(p.ws + OFF_LIST) + (size_t)mu.e * NTOK; const int i0 = mu.mt * 256, col0 = mu.nt * 256;
;         const unsigned ao = (unsigned)((T.aR * D + T.aC) * 2), bo = (unsigned)((T.b_k * D + T.b_col) * 4);
;         int pa = -1; float pg = 0.f;
;         { const int t_ = tid_opaque(); if (t_ < 256 && i0 + t_ < mu.cnt) { pa = list[i0 + t_]; pg = gate[pa]; } }
;         f32x4 acc[8][4]; acc_zero(acc);
;         const int mlim = __builtin_amdgcn_readfirstlane(T.wr) ? 0 : ((mu.cnt - i0 + 15) >> 4);
;         if (mu.light) gemm_kloop_light(acc, lds, T, mk_rsrc(act + (size_t)(mu.base + i0) * D), ao, ao + 64u * 4096, ao + 128u * 4096, ao + 192u * 4096,
;                                        mk_rsrc(p.w_down + (size_t)mu.e * D * D + col0), bo, D * 4u, D / 64, mlim);
;         else gemm_kloop(acc, lds, T, mk_rsrc(act + (size_t)(mu.base + i0) * D), ao, ao + 64u * 4096, ao + 128u * 4096, ao + 192u * 4096,
;                         mk_rsrc(p.w_down + (size_t)mu.e * D * D + col0), bo, D * 4u, D / 64);
.LBB0_1483:
	s_or_b64 exec, exec, s[0:1]
	s_add_i32 s2, s84, s85
	s_ashr_i32 s3, s2, 31
	s_lshl_b32 s0, s81, 8
	s_lshl_b64 s[2:3], s[2:3], 12
	s_add_u32 s36, s20, s2
	v_readlane_b32 s4, v246, 0
	s_addc_u32 s1, s28, s3
	v_readlane_b32 s5, v246, 1
	v_readlane_b32 s6, v246, 2
	v_readlane_b32 s7, v246, 3
	v_readlane_b32 s8, v246, 4
	v_readlane_b32 s9, v246, 5
	s_and_b32 s37, s1, 0xffff
	s_lshl_b64 s[2:3], s[42:43], 24
	v_readlane_b32 s10, v246, 6
	v_readlane_b32 s11, v246, 7
	s_mov_b64 s[4:5], s[8:9]
	s_add_u32 s4, s4, s2
	v_ashrrev_i32_e32 v4, 6, v3
	v_bfe_u32 v11, v3, 1, 2
	s_addc_u32 s5, s5, s3
	s_ashr_i32 s1, s0, 31
	v_ashrrev_i32_e32 v5, 7, v3
	v_and_b32_e32 v6, 1, v4
	v_bfe_u32 v8, v3, 5, 1
	v_bfe_u32 v10, v3, 3, 2
	v_and_b32_e32 v12, 1, v3
	v_lshlrev_b32_e32 v14, 3, v11
	s_lshl_b64 s[2:3], s[0:1], 2
	v_lshlrev_b32_e32 v7, 5, v6
	v_lshl_or_b32 v9, v5, 1, v8
	v_lshl_or_b32 v14, v10, 6, v14
	v_lshlrev_b32_e32 v15, 2, v12
	s_add_u32 s24, s4, s2
	v_lshlrev_b32_e32 v13, 16, v9
	v_or3_b32 v14, v14, v15, v7
	s_addc_u32 s1, s5, s3
	v_lshl_or_b32 v222, v14, 2, v13
	s_and_b32 s25, s1, 0xffff
	s_movk_i32 s1, 0x2000
	buffer_load_dwordx4 v[110:113], v222, s[24:27], 0 offen
	buffer_load_dwordx4 v[114:117], v222, s[24:27], s66 offen
	s_mov_b32 s2, 0x8000
	buffer_load_dwordx4 v[122:125], v222, s[24:27], s1 offen
	buffer_load_dwordx4 v[118:121], v222, s[24:27], s2 offen
	s_movk_i32 s1, 0x4000
	s_mov_b32 s2, 0xa000
	buffer_load_dwordx4 v[126:129], v222, s[24:27], s1 offen
	buffer_load_dwordx4 v[130:133], v222, s[24:27], s2 offen
	s_mov_b32 s1, 0xc000
	s_mov_b32 s2, 0xe000
	buffer_load_dwordx4 v[138:141], v222, s[24:27], s1 offen
	buffer_load_dwordx4 v[142:145], v222, s[24:27], s2 offen
	s_waitcnt vmcnt(8)
	v_cmp_ne_u32_e32 vcc, -1, v214
	s_and_saveexec_b64 vcc, vcc
	v_ashrrev_i32_e32 v17, 31, v214
	v_mov_b32_e32 v16, v214
	v_lshl_add_u64 v[16:17], v[16:17], 2, s[56:57]
	global_load_dword v215, v[16:17], off
	s_or_b64 exec, exec, vcc
	v_lshlrev_b32_e32 v16, 3, v3
	v_and_b32_e32 v13, 63, v3
	v_lshlrev_b32_e32 v8, 4, v8
	v_and_b32_e32 v17, 24, v16
	v_bitop3_b32 v7, v8, v7, v17 bitop3:0xde
	v_lshlrev_b32_e32 v8, 4, v13
	v_lshl_or_b32 v230, v4, 10, v8
	v_lshlrev_b32_e32 v8, 2, v10
	v_lshlrev_b32_e32 v6, 1, v6
	v_or3_b32 v6, v8, v6, v12
	v_lshlrev_b32_e32 v8, 2, v3
	v_and_b32_e32 v10, 0xfffffc00, v8
	v_lshl_add_u32 v6, v6, 11, v10
	v_lshlrev_b32_e32 v10, 8, v11
	v_lshlrev_b32_e32 v9, 4, v9
	v_and_b32_e32 v15, 15, v3
	v_and_or_b32 v9, v9, 48, v10
	v_and_b32_e32 v10, 32, v16
	v_bitop3_b32 v220, v6, v9, v10 bitop3:0xf6
	v_lshlrev_b32_e32 v6, 6, v15
	v_and_b32_e32 v9, 48, v3
	v_and_b32_e32 v8, 32, v8
	v_or_b32_e32 v10, v6, v9
	v_bitop3_b32 v6, v6, v8, v9 bitop3:0x36
	v_lshlrev_b32_e32 v4, 13, v4
	v_ashrrev_i32_e32 v14, 8, v3
	v_and_or_b32 v227, v4, s66, v6
	v_lshlrev_b32_e32 v4, 16, v5
	v_lshlrev_b32_e32 v3, 10, v3
	s_mov_b32 s1, 0xf000
	v_lshlrev_b32_e32 v219, 6, v12
	v_and_or_b32 v3, v3, s1, v4
	v_lshlrev_b32_e32 v9, 14, v14
	v_lshl_or_b32 v225, v7, 1, v3
	v_cmp_eq_u32_e32 vcc, 0, v216
	v_add_u32_e32 v228, 0, v220
	v_add_u32_e32 v3, 0xc0, v219
	v_bitop3_b32 v217, v10, v9, v8 bitop3:0xde
	v_or_b32_e32 v218, 0x8000, v227
	v_readfirstlane_b32 s1, v14
	v_add_u32_e32 v226, 0x40000, v225
	v_add_u32_e32 v224, 0x80000, v225
	v_add_u32_e32 v223, 0xc0000, v225
	v_add_u32_e32 v229, v228, v219
	v_and_b32_e32 v221, 0xc0, v3
	s_mov_b64 s[6:7], s[10:11]
	s_cbranch_vccnz .LBB0_1574
; #define G_DMA_A(buf, t, i_) __builtin_amdgcn_raw_ptr_buffer_load_lds(ra, (LAS void*)(lds + (buf) * 65536 + a_wu + (i_) * 8192), 16, ao##i_, (unsigned)(t) * 128u, 0, 0)
; #define G_ISSUE_B(t) do { const unsigned so_ = (unsigned)(t) * 64u * ldbB; _Pragma("unroll") for (int i_ = 0; i_ < 8; ++i_) sb[i_] = __builtin_bit_cast(f32x4, __builtin_amdgcn_raw_buffer_load_b128(rb, bo, so_ + (unsigned)i_ * ldbB, 0)); } while (0)
; #define G_RETIRE() asm volatile("s_waitcnt vmcnt(0)" : "+v"(sb[0]), "+v"(sb[1]), "+v"(sb[2]), "+v"(sb[3]), "+v"(sb[4]), "+v"(sb[5]), "+v"(sb[6]), "+v"(sb[7]) :: "memory")
; #define G_WRITE_B(buf) do { LAS unsigned char* d_ = lds + (buf) * 65536; \
;         _Pragma("unroll") for (int j_ = 0; j_ < 4; ++j_) { u32x4 w_; w_.x = cvtpk(sb[0][j_], sb[1][j_]); w_.y = cvtpk(sb[2][j_], sb[3][j_]); w_.z = cvtpk(sb[4][j_], sb[5][j_]); w_.w = cvtpk(sb[6][j_], sb[7][j_]); \
;             *(LAS u32x4*)(d_ + 32768 + T.b_w + ((T.b_rot + 64u * j_) & 255u)) = w_; } } while (0)
; #define G_BAR() do { asm volatile("s_waitcnt lgkmcnt(0)" ::: "memory"); __builtin_amdgcn_s_barrier(); asm volatile("" ::: "memory"); } while (0)
; #define G_DMA_A(buf, t, i_) __builtin_amdgcn_raw_ptr_buffer_load_lds(ra, (LAS void*)(lds + (buf) * 65536 + a_wu + (i_) * 8192), 16, ao##i_, (unsigned)(t) * 128u, 0, 0)
; #define G_ISSUE_B(t) do { const unsigned so_ = (unsigned)(t) * 64u * ldbB; _Pragma("unroll") for (int i_ = 0; i_ < 8; ++i_) sb[i_] = __builtin_bit_cast(f32x4, __builtin_amdgcn_raw_buffer_load_b128(rb, bo, so_ + (unsigned)i_ * ldbB, 0)); } while (0)
; #define G_RETIRE() asm volatile("s_waitcnt vmcnt(0)" : "+v"(sb[0]), "+v"(sb[1]), "+v"(sb[2]), "+v"(sb[3]), "+v"(sb[4]), "+v"(sb[5]), "+v"(sb[6]), "+v"(sb[7]) :: "memory")
; __device__ __forceinline__ void gemm_kloop_light(f32x4 (&acc)[8][4], LAS unsigned char* lds, const GemmT& T, ...
;     ...
;     G_ISSUE_B(0); G_DMA_A(0, 0, 0); G_DMA_A(0, 0, 1); G_DMA_A(0, 0, 2); G_DMA_A(0, 0, 3); G_RETIRE(); G_WRITE_B(0);
;     if (nt > 1) G_ISSUE_B(1);
;     G_BAR();
; __device__ __forceinline__ void phase_moe_down(const Ptrs& p, LAS unsigned char* lds) {
;     ...
;         f32x4 acc[8][4]; acc_zero(acc);
;         const int mlim = __builtin_amdgcn_readfirstlane(T.wr) ? 0 : ((mu.cnt - i0 + 15) >> 4);
	s_sub_i32 s2, s83, s85
	s_mov_b32 s99, s2
	v_readfirstlane_b32 s100, v0
	s_nop 3
	s_lshr_b32 s100, s100, 7
	s_lshl_b32 s100, s100, 4
	s_add_i32 s2, s2, 15
	s_ashr_i32 s2, s2, 4
	s_cmp_eq_u32 s1, 0
	s_cselect_b32 s1, s2, 0
	v_readfirstlane_b32 s2, v230
	s_and_b32 s2, s2, 0xfffffc00
	s_add_i32 s2, s2, 0
	s_mov_b32 s38, s26
	s_mov_b32 s39, s27
	s_mov_b32 m0, s2
	s_waitcnt vmcnt(4)
	v_mov_b64_e32 v[4:5], v[118:119]
	buffer_load_dwordx4 v225, s[36:39], 0 offen lds
	s_add_i32 m0, s2, 0x2000
	s_waitcnt vmcnt(2)
	v_mov_b64_e32 v[8:9], v[138:139]
	buffer_load_dwordx4 v226, s[36:39], 0 offen lds
	s_add_i32 m0, s2, 0x4000
	v_mov_b64_e32 v[12:13], v[122:123]
	buffer_load_dwordx4 v224, s[36:39], 0 offen lds
	s_add_i32 m0, s2, 0x6000
	v_mov_b64_e32 v[16:17], v[114:115]
	v_mov_b64_e32 v[20:21], v[130:131]
	v_mov_b64_e32 v[24:25], v[110:111]
	s_waitcnt vmcnt(3)
	v_mov_b64_e32 v[28:29], v[142:143]
	v_mov_b64_e32 v[32:33], v[126:127]
	buffer_load_dwordx4 v223, s[36:39], 0 offen lds
	v_mov_b64_e32 v[6:7], v[120:121]
	v_mov_b64_e32 v[10:11], v[140:141]
	v_mov_b64_e32 v[14:15], v[124:125]
	v_mov_b64_e32 v[18:19], v[116:117]
	v_mov_b64_e32 v[22:23], v[132:133]
	v_mov_b64_e32 v[26:27], v[112:113]
	v_mov_b64_e32 v[30:31], v[144:145]
	v_mov_b64_e32 v[34:35], v[128:129]
	s_waitcnt vmcnt(0)
	buffer_load_dwordx4 v[162:165], v222, s[24:27], s67 offen
	buffer_load_dwordx4 v[170:173], v222, s[24:27], s68 offen
	buffer_load_dwordx4 v[174:177], v222, s[24:27], s69 offen
	buffer_load_dwordx4 v[178:181], v222, s[24:27], s70 offen
	buffer_load_dwordx4 v[182:185], v222, s[24:27], s71 offen
	buffer_load_dwordx4 v[186:189], v222, s[24:27], s76 offen
	buffer_load_dwordx4 v[190:193], v222, s[24:27], s77 offen
	buffer_load_dwordx4 v[194:197], v222, s[24:27], s78 offen
	s_cmp_gt_i32 s1, 0
	s_cselect_b64 s[60:61], -1, 0
	s_cmp_lg_u32 s1, 1
	v_cvt_pk_bf16_f32 v36, v24, v12
	v_cvt_pk_bf16_f32 v37, v32, v16
	v_cvt_pk_bf16_f32 v38, v4, v20
	v_cvt_pk_bf16_f32 v39, v8, v28
	s_cselect_b64 s[58:59], -1, 0
	s_cmp_gt_i32 s1, 2
	ds_write_b128 v229, v[36:39] offset:32768
	v_cvt_pk_bf16_f32 v36, v25, v13
	v_cvt_pk_bf16_f32 v37, v33, v17
	v_cvt_pk_bf16_f32 v38, v5, v21
	v_cvt_pk_bf16_f32 v39, v9, v29
	s_cselect_b64 s[54:55], -1, 0
	s_cmp_gt_i32 s1, 3
	ds_write_b128 v229, v[36:39] offset:32832
	v_cvt_pk_bf16_f32 v36, v26, v14
	v_cvt_pk_bf16_f32 v37, v34, v18
	v_cvt_pk_bf16_f32 v38, v6, v22
	v_cvt_pk_bf16_f32 v39, v10, v30
	v_cvt_pk_bf16_f32 v4, v27, v15
	v_cvt_pk_bf16_f32 v5, v35, v19
	v_cvt_pk_bf16_f32 v6, v7, v23
	v_cvt_pk_bf16_f32 v7, v11, v31
	v_add_u32_e32 v3, v228, v221
	s_cselect_b64 s[50:51], -1, 0
	s_cmp_gt_i32 s1, 4
	ds_write_b128 v229, v[36:39] offset:32896
	ds_write_b128 v3, v[4:7] offset:32768
	s_cselect_b64 s[48:49], -1, 0
	s_cmp_gt_i32 s1, 5
	s_waitcnt lgkmcnt(0)
	s_barrier
	s_cselect_b64 s[46:47], -1, 0
	s_cmp_gt_i32 s1, 6
	v_mov_b32_e32 v4, v2
	v_mov_b32_e32 v5, v2
	s_cselect_b64 s[44:45], -1, 0
	s_cmp_gt_i32 s1, 7
	v_mov_b32_e32 v3, v2
	v_mov_b64_e32 v[12:13], v[4:5]
	v_mov_b64_e32 v[8:9], v[4:5]
	v_mov_b64_e32 v[20:21], v[4:5]
	v_mov_b64_e32 v[16:17], v[4:5]
	v_mov_b64_e32 v[28:29], v[4:5]
	v_mov_b64_e32 v[24:25], v[4:5]
	v_mov_b64_e32 v[36:37], v[4:5]
	v_mov_b64_e32 v[32:33], v[4:5]
	v_mov_b64_e32 v[44:45], v[4:5]
	v_mov_b64_e32 v[40:41], v[4:5]
	v_mov_b64_e32 v[52:53], v[4:5]
	v_mov_b64_e32 v[48:49], v[4:5]
	v_mov_b64_e32 v[60:61], v[4:5]
	v_mov_b64_e32 v[56:57], v[4:5]
	v_mov_b64_e32 v[68:69], v[4:5]
	v_mov_b64_e32 v[64:65], v[4:5]
	v_mov_b64_e32 v[76:77], v[4:5]
	v_mov_b64_e32 v[72:73], v[4:5]
	v_mov_b64_e32 v[84:85], v[4:5]
	v_mov_b64_e32 v[80:81], v[4:5]
	v_mov_b64_e32 v[92:93], v[4:5]
	v_mov_b64_e32 v[88:89], v[4:5]
	v_mov_b64_e32 v[100:101], v[4:5]
	v_mov_b64_e32 v[96:97], v[4:5]
	v_mov_b64_e32 v[108:109], v[4:5]
	v_mov_b64_e32 v[104:105], v[4:5]
	v_mov_b64_e32 v[148:149], v[4:5]
	v_mov_b64_e32 v[136:137], v[4:5]
	v_mov_b64_e32 v[156:157], v[4:5]
	v_mov_b64_e32 v[152:153], v[4:5]
	v_mov_b64_e32 v[168:169], v[4:5]
	v_mov_b64_e32 v[160:161], v[4:5]
	s_mov_b32 s3, 0
	s_cselect_b64 s[34:35], -1, 0
	s_mov_b32 s72, 0x10e000
	s_movk_i32 s73, 0x80
	v_mov_b64_e32 v[10:11], v[2:3]
	v_mov_b64_e32 v[6:7], v[2:3]
	v_mov_b64_e32 v[18:19], v[2:3]
	v_mov_b64_e32 v[14:15], v[2:3]
	v_mov_b64_e32 v[26:27], v[2:3]
	v_mov_b64_e32 v[22:23], v[2:3]
	v_mov_b64_e32 v[34:35], v[2:3]
	v_mov_b64_e32 v[30:31], v[2:3]
	v_mov_b64_e32 v[42:43], v[2:3]
	v_mov_b64_e32 v[38:39], v[2:3]
	v_mov_b64_e32 v[50:51], v[2:3]
	v_mov_b64_e32 v[46:47], v[2:3]
	v_mov_b64_e32 v[58:59], v[2:3]
	v_mov_b64_e32 v[54:55], v[2:3]
	v_mov_b64_e32 v[66:67], v[2:3]
	v_mov_b64_e32 v[62:63], v[2:3]
	v_mov_b64_e32 v[74:75], v[2:3]
	v_mov_b64_e32 v[70:71], v[2:3]
	v_mov_b64_e32 v[82:83], v[2:3]
	v_mov_b64_e32 v[78:79], v[2:3]
	v_mov_b64_e32 v[90:91], v[2:3]
	v_mov_b64_e32 v[86:87], v[2:3]
	v_mov_b64_e32 v[98:99], v[2:3]
	v_mov_b64_e32 v[94:95], v[2:3]
	v_mov_b64_e32 v[106:107], v[2:3]
	v_mov_b64_e32 v[102:103], v[2:3]
	v_mov_b64_e32 v[146:147], v[2:3]
	v_mov_b64_e32 v[134:135], v[2:3]
	v_mov_b64_e32 v[154:155], v[2:3]
	v_mov_b64_e32 v[150:151], v[2:3]
	v_mov_b64_e32 v[166:167], v[2:3]
	v_mov_b64_e32 v[158:159], v[2:3]
	s_branch .LBB0_1486

; #define G_DMA_A(buf, t, i_) __builtin_amdgcn_raw_ptr_buffer_load_lds(ra, (LAS void*)(lds + (buf) * 65536 + a_wu + (i_) * 8192), 16, ao##i_, (unsigned)(t) * 128u, 0, 0)
; #define G_DMA_A(buf, t, i_) __builtin_amdgcn_raw_ptr_buffer_load_lds(ra, (LAS void*)(lds + (buf) * 65536 + a_wu + (i_) * 8192), 16, ao##i_, (unsigned)(t) * 128u, 0, 0)
; __device__ __forceinline__ void gemm_kloop_light(f32x4 (&acc)[8][4], LAS unsigned char* lds, const GemmT& T, ...
;     ...
;     for (int t = 0; t < nt; ++t) { const int cur = t & 1; const bool w1 = t + 1 < nt, i2 = t + 2 < nt;
;         if (w1) { G_DMA_A(cur ^ 1, t + 1, 0); G_DMA_A(cur ^ 1, t + 1, 1); G_DMA_A(cur ^ 1, t + 1, 2); G_DMA_A(cur ^ 1, t + 1, 3); }
;         if (mlim > 0) {
.LBB0_1486:
	s_and_b32 s6, s3, 0x10000
	s_xor_b32 s74, s6, 0x10000
	s_add_i32 s4, s2, s74
	s_mov_b32 m0, s4
	s_add_i32 s5, s4, 0x6000
	s_add_i32 s7, s4, 0x4000
	s_addk_i32 s4, 0x2000
	s_cmp_le_i32 s99, s100
	s_cbranch_scc1 .Lmy_lsz2
	buffer_load_dwordx4 v225, s[36:39], s73 offen lds
.Lmy_lsz2:
	s_mov_b32 m0, s4
	v_cndmask_b32_e64 v3, 0, 1, s[60:61]
	s_cmp_lt_i32 s99, 65
	s_cbranch_scc1 .Lmy_lsk2
	buffer_load_dwordx4 v226, s[36:39], s73 offen lds

; #define G_DMA_A(buf, t, i_) __builtin_amdgcn_raw_ptr_buffer_load_lds(ra, (LAS void*)(lds + (buf) * 65536 + a_wu + (i_) * 8192), 16, ao##i_, (unsigned)(t) * 128u, 0, 0)
; #define G_DMA_A(buf, t, i_) __builtin_amdgcn_raw_ptr_buffer_load_lds(ra, (LAS void*)(lds + (buf) * 65536 + a_wu + (i_) * 8192), 16, ao##i_, (unsigned)(t) * 128u, 0, 0)
; __device__ __forceinline__ void gemm_kloop_light(f32x4 (&acc)[8][4], LAS unsigned char* lds, const GemmT& T, ...
;     ...
;     for (int t = 0; t < nt; ++t) { const int cur = t & 1; const bool w1 = t + 1 < nt, i2 = t + 2 < nt;
;         if (w1) { G_DMA_A(cur ^ 1, t + 1, 0); G_DMA_A(cur ^ 1, t + 1, 1); G_DMA_A(cur ^ 1, t + 1, 2); G_DMA_A(cur ^ 1, t + 1, 3); }
;         if (mlim > 0) {
.LBB0_1515:
	s_add_i32 m0, s2, 0x10000
	s_add_i32 s3, s2, 0x16000
	s_add_i32 s6, s2, 0x14000
	s_add_i32 s2, s2, 0x12000
	s_mov_b32 s38, s26
	s_mov_b32 s39, s27
	s_cmp_le_i32 s99, s100
	s_cbranch_scc1 .Lmy_lsz3
	buffer_load_dwordx4 v225, s[36:39], s79 offen lds
.Lmy_lsz3:
	s_mov_b32 m0, s2
	v_cndmask_b32_e64 v3, 0, 1, s[58:59]
	s_cmp_lt_i32 s99, 65
	s_cbranch_scc1 .Lmy_lsk3
	buffer_load_dwordx4 v226, s[36:39], s79 offen lds
